# grid barrier: one acquire (buffer_inv sc1) per compute unit - the first-arrived workgroup of a CU invalidates and sets a per-CU flag word, its co-resident workgroup waits for the flag instead of inval
# speedup vs baseline: 1.0199x; 1.0132x over previous
; __device__ __forceinline__ unsigned xb_ld(unsigned* p)              { return __hip_atomic_load(p, __ATOMIC_RELAXED, __HIP_MEMORY_SCOPE_AGENT); }
; __device__ __forceinline__ unsigned xb_add(unsigned* p, unsigned v) { return __hip_atomic_fetch_add(p, v, __ATOMIC_RELAXED, __HIP_MEMORY_SCOPE_AGENT); }
; #define XB_SPIN(cond, bar) do { unsigned _sp = 0; while (cond) { __builtin_amdgcn_s_sleep(1); \
;     if ((++_sp & 255u) == 0u) { if (xb_ld(&(bar)[XB_TMO])) break; if (_sp > XB_SPIN_CAP) { atomicAdd(&(bar)[XB_TMO], 1u); break; } } } } while (0)
; __device__ __forceinline__ void xcd_barrier(const XcdBarrier& b) {
;     ...
;             __builtin_amdgcn_fence(__ATOMIC_ACQUIRE, "agent");
;             xb_add(&bar[XB_XGEN(b.x)], 1u);
;             asm volatile("s_waitcnt vmcnt(0)" ::: "memory");
;         } else {
;             XB_SPIN(xb_ld(&bar[XB_XGEN(b.x)]) == gen, bar);
;             __builtin_amdgcn_fence(__ATOMIC_ACQUIRE, "agent");
;             asm volatile("s_waitcnt vmcnt(0)" ::: "memory");
;         }
.Lxb_notlast:
	s_or_b64 exec, exec, s[28:29]
	ds_read_b32 v7, v146
	s_getreg_b32 s28, hwreg(HW_REG_XCC_ID, 0, 4)
	s_getreg_b32 s29, hwreg(HW_REG_HW_ID, 8, 8)
	v_readlane_b32 s44, v252, 44
	v_readlane_b32 s45, v252, 45
	s_lshl_b32 s28, s28, 8
	s_and_b32 s28, s28, 0xf00
	s_and_b32 s29, s29, 0xff
	s_or_b32 s28, s28, s29
	s_lshl_b32 s28, s28, 6
	s_add_u32 s28, s28, 0x38c00
	s_add_u32 s44, s44, s28
	s_addc_u32 s45, s45, 0
	s_mov_b32 s15, 0
	s_waitcnt lgkmcnt(0)
	v_readfirstlane_b32 s29, v7
	s_cmp_lg_u32 s29, 0
	s_cbranch_scc1 .Lxb_poll_cu

; __device__ __forceinline__ unsigned xb_ld(unsigned* p)              { return __hip_atomic_load(p, __ATOMIC_RELAXED, __HIP_MEMORY_SCOPE_AGENT); }
; __device__ __forceinline__ unsigned xb_add(unsigned* p, unsigned v) { return __hip_atomic_fetch_add(p, v, __ATOMIC_RELAXED, __HIP_MEMORY_SCOPE_AGENT); }
; #define XB_SPIN(cond, bar) do { unsigned _sp = 0; while (cond) { __builtin_amdgcn_s_sleep(1); \
;     if ((++_sp & 255u) == 0u) { if (xb_ld(&(bar)[XB_TMO])) break; if (_sp > XB_SPIN_CAP) { atomicAdd(&(bar)[XB_TMO], 1u); break; } } } } while (0)
; __device__ __forceinline__ void xcd_barrier(const XcdBarrier& b) {
;     ...
;             __builtin_amdgcn_fence(__ATOMIC_ACQUIRE, "agent");
;             xb_add(&bar[XB_XGEN(b.x)], 1u);
;             asm volatile("s_waitcnt vmcnt(0)" ::: "memory");
;         } else {
;             XB_SPIN(xb_ld(&bar[XB_XGEN(b.x)]) == gen, bar);
;             __builtin_amdgcn_fence(__ATOMIC_ACQUIRE, "agent");
;             asm volatile("s_waitcnt vmcnt(0)" ::: "memory");
;         }
.Lxb_done:
	s_waitcnt vmcnt(0) lgkmcnt(0)
	buffer_inv sc1
	s_waitcnt vmcnt(0)
	global_store_dword v3, v255, s[44:45]
	s_branch .Lxb_out
.Lxb_poll_cu:
	global_load_dword v6, v3, s[44:45] sc1
	s_waitcnt vmcnt(0)
	v_cmp_ge_u32_e32 vcc, v6, v255
	s_cbranch_vccnz .Lxb_out
	s_add_i32 s15, s15, 1
	s_cmp_lt_u32 s15, 0x400000
	s_cbranch_scc1 .Lxb_poll_cu
.Lxb_out:
	s_mov_b64 s[28:29], exec
	s_getpc_b64 s[98:99]
